# v11: v10 plus phase-9 group-1 alignment barrier deferred past the next unit's set-up code (set-up of both groups overlaps)
# speedup vs baseline: 1.0050x; 1.0012x over previous
.LBB0_1321:
	s_cmp_lt_i32 s52, 10
	s_cselect_b64 s[0:1], -1, 0
	s_cmp_gt_i32 s53, 9
	s_cselect_b64 s[2:3], -1, 0
	s_and_b64 s[0:1], s[0:1], s[2:3]
	s_andn2_b64 vcc, exec, s[0:1]
	s_cbranch_vccnz .LBB0_1504
	s_mov_b32 s100, 0
	s_waitcnt vmcnt(0)
	v_mov_b32_e32 v3, v0
	s_nop 0
	v_cmp_gt_i32_e32 vcc, 64, v3
	s_and_saveexec_b64 s[0:1], vcc
	s_cbranch_execz .LBB0_1339
	v_and_b32_e32 v1, 31, v3
	v_lshlrev_b32_e32 v4, 2, v1
	v_mov_b32_e32 v5, 0
	v_lshl_add_u64 v[4:5], s[96:97], 0, v[4:5]
	v_add_co_u32_e32 v4, vcc, 0xc000, v4
	s_nop 1
	v_addc_co_u32_e32 v5, vcc, 0, v5, vcc
	global_load_dword v2, v[4:5], off sc1
	v_mbcnt_lo_u32_b32 v4, -1, 0
	v_mbcnt_hi_u32_b32 v5, -1, v4
	v_and_b32_e32 v6, 0x60, v5
	v_add_u32_e32 v4, -1, v5
	v_cmp_lt_i32_e32 vcc, v4, v6
	v_add_u32_e32 v7, -2, v5
	v_add_u32_e32 v8, -4, v5
	v_cndmask_b32_e32 v4, v4, v5, vcc
	v_lshlrev_b32_e32 v10, 2, v4
	v_cmp_lt_i32_e32 vcc, v7, v6
	v_add_u32_e32 v9, -8, v5
	s_waitcnt vmcnt(0)
	v_add_u32_e32 v4, 0xff, v2
	v_ashrrev_i32_e32 v2, 31, v4
	v_add_u32_sdwa v2, v4, v2 dst_sel:DWORD dst_unused:UNUSED_PAD src0_sel:DWORD src1_sel:BYTE_3
	v_ashrrev_i32_e32 v2, 8, v2
	ds_bpermute_b32 v10, v10, v2
	v_cndmask_b32_e32 v7, v7, v5, vcc
	v_cmp_ne_u32_e32 vcc, 0, v1
	v_lshlrev_b32_e32 v7, 2, v7
	s_waitcnt lgkmcnt(0)
	v_cndmask_b32_e32 v10, 0, v10, vcc
	v_add_u32_e32 v10, v10, v2
	ds_bpermute_b32 v7, v7, v10
	v_cmp_lt_i32_e32 vcc, v8, v6
	s_nop 1
	v_cndmask_b32_e32 v8, v8, v5, vcc
	v_cmp_lt_u32_e32 vcc, 1, v1
	v_lshlrev_b32_e32 v8, 2, v8
	s_waitcnt lgkmcnt(0)
	v_cndmask_b32_e32 v7, 0, v7, vcc
	v_add_u32_e32 v7, v7, v10
	ds_bpermute_b32 v8, v8, v7
	v_cmp_lt_i32_e32 vcc, v9, v6
	s_nop 1
	v_cndmask_b32_e32 v9, v9, v5, vcc
	v_cmp_lt_u32_e32 vcc, 3, v1
	v_lshlrev_b32_e32 v9, 2, v9
	s_waitcnt lgkmcnt(0)
	v_cndmask_b32_e32 v8, 0, v8, vcc
	v_add_u32_e32 v7, v8, v7
	ds_bpermute_b32 v8, v9, v7
	v_add_u32_e32 v9, -16, v5
	v_cmp_lt_i32_e32 vcc, v9, v6
	s_nop 1
	v_cndmask_b32_e32 v6, v9, v5, vcc
	v_cmp_lt_u32_e32 vcc, 7, v1
	v_lshlrev_b32_e32 v6, 2, v6
	s_waitcnt lgkmcnt(0)
	v_cndmask_b32_e32 v5, 0, v8, vcc
	v_add_u32_e32 v5, v5, v7
	ds_bpermute_b32 v6, v6, v5
	v_cmp_gt_i32_e32 vcc, 32, v3
	s_and_b64 exec, exec, vcc
	s_cbranch_execz .LBB0_1339
	v_cmp_lt_u32_e32 vcc, 15, v1
	v_lshl_add_u32 v7, v1, 2, 0
	v_add_u32_e32 v7, 0x21000, v7
	s_waitcnt lgkmcnt(0)
	v_cndmask_b32_e32 v3, 0, v6, vcc
	v_add_u32_e32 v5, v3, v5
	v_sub_u32_e32 v3, v5, v2
	v_lshlrev_b32_e32 v6, 8, v3
	v_cmp_eq_u32_e32 vcc, 31, v1
	ds_write_b32 v7, v6
	s_and_saveexec_b64 s[2:3], vcc
	s_add_i32 s4, 0, 0x21080
	v_lshlrev_b32_e32 v5, 8, v5
	v_mov_b32_e32 v6, s4
	ds_write_b32 v6, v5
	s_or_b64 exec, exec, s[2:3]
	s_movk_i32 s2, 0xff
	v_cmp_lt_i32_e32 vcc, s2, v4
	s_and_b64 exec, exec, vcc
	s_cbranch_execz .LBB0_1339
	v_cmp_lt_u32_e32 vcc, 1, v2
	s_mov_b64 s[4:5], -1
	v_mov_b32_e32 v4, 0
	s_and_saveexec_b64 s[2:3], vcc
	s_cbranch_execz .LBB0_1336
	v_add_u32_e32 v5, -2, v2
	v_lshrrev_b32_e32 v4, 1, v5
	v_add_u32_e32 v4, 1, v4
	v_cmp_lt_u32_e32 vcc, 13, v5
	v_mov_b32_e32 v7, 0
	s_and_saveexec_b64 s[4:5], vcc
	s_cbranch_execz .LBB0_1332
	v_lshl_add_u32 v6, v3, 2, 0
	v_and_b32_e32 v5, -8, v4
	s_mov_b32 s8, 0
	v_add_u32_e32 v6, 0x20000, v6
	s_mov_b64 s[6:7], 0

.LBB0_1441:
	s_cmp_eq_u32 s100, 0
	s_cbranch_scc1 .Lz1b_1442
	v_readfirstlane_b32 s99, v0
	s_cmpk_gt_u32 s99, 0xff
	s_cbranch_scc0 .Lz1b_1442
	s_barrier

.Lz0_1442:
	v_pk_fma_f32 v[130:131], v[134:135], v[130:131], v[130:131]
	v_pk_mul_f32 v[134:135], v[16:17], s[34:35] op_sel_hi:[1,0]
	v_pk_add_f32 v[136:137], v[136:137], 1.0 op_sel_hi:[1,0]
	v_exp_f32_e32 v134, v134
	v_exp_f32_e32 v135, v135
	v_rcp_f32_e32 v136, v136
	v_rcp_f32_e32 v137, v137
	v_med3_f32 v132, v132, s65, v179
	v_pk_add_f32 v[134:135], v[134:135], 1.0 op_sel_hi:[1,0]
	v_med3_f32 v133, v133, s65, v179
	v_pk_mul_f32 v[130:131], v[130:131], v[136:137]
	v_rcp_f32_e32 v134, v134
	v_rcp_f32_e32 v135, v135
	v_mov_b32_e32 v137, v167
	v_cvt_pk_fp8_f32 v137, v130, v131
	v_mov_b32_e32 v136, v167
	v_cvt_pk_fp8_f32 v136, v14, v15
	v_pk_fma_f32 v[14:15], v[132:133], v[16:17], v[16:17]
	v_pk_fma_f32 v[114:115], v[114:115], s[30:31], v[22:23] op_sel_hi:[1,0,1]
	v_pk_mul_f32 v[14:15], v[14:15], v[134:135]
	v_cvt_pk_fp8_f32 v136, v12, v13 op_sel:[0,0,1]
	v_cvt_pk_fp8_f32 v137, v14, v15 op_sel:[0,0,1]
	v_pk_fma_f32 v[14:15], v[122:123], s[30:31], v[30:31] op_sel_hi:[1,0,1]
	v_pk_fma_f32 v[12:13], v[124:125], s[30:31], v[32:33] op_sel_hi:[1,0,1]
	v_min_f32_e32 v14, 0x40e00000, v14
	v_min_f32_e32 v15, 0x40e00000, v15
	v_pk_mul_f32 v[16:17], v[14:15], s[34:35] op_sel_hi:[1,0]
	v_min_f32_e32 v12, 0x40e00000, v12
	v_exp_f32_e32 v16, v16
	v_exp_f32_e32 v17, v17
	v_min_f32_e32 v13, 0x40e00000, v13
	v_pk_fma_f32 v[124:125], v[126:127], s[30:31], v[26:27] op_sel_hi:[1,0,1]
	v_pk_mul_f32 v[126:127], v[12:13], s[34:35] op_sel_hi:[1,0]
	v_pk_add_f32 v[16:17], v[16:17], 1.0 op_sel_hi:[1,0]
	v_exp_f32_e32 v126, v126
	v_rcp_f32_e32 v16, v16
	v_rcp_f32_e32 v17, v17
	v_exp_f32_e32 v127, v127
	v_med3_f32 v124, v124, s65, v179
	v_med3_f32 v125, v125, s65, v179
	v_pk_fma_f32 v[14:15], v[124:125], v[14:15], v[14:15]
	v_pk_fma_f32 v[122:123], v[128:129], s[30:31], v[28:29] op_sel_hi:[1,0,1]
	v_pk_mul_f32 v[14:15], v[14:15], v[16:17]
	v_pk_add_f32 v[16:17], v[126:127], 1.0 op_sel_hi:[1,0]
	v_med3_f32 v122, v122, s65, v179
	v_rcp_f32_e32 v16, v16
	v_rcp_f32_e32 v17, v17
	v_med3_f32 v123, v123, s65, v179
	v_pk_fma_f32 v[12:13], v[122:123], v[12:13], v[12:13]
	v_min_f32_e32 v114, 0x40e00000, v114
	v_min_f32_e32 v115, 0x40e00000, v115
	v_pk_mul_f32 v[12:13], v[12:13], v[16:17]
	v_pk_fma_f32 v[16:17], v[116:117], s[30:31], v[24:25] op_sel_hi:[1,0,1]
	v_pk_fma_f32 v[116:117], v[120:121], s[30:31], v[20:21] op_sel_hi:[1,0,1]
	v_pk_mul_f32 v[120:121], v[114:115], s[34:35] op_sel_hi:[1,0]
	v_pk_fma_f32 v[118:119], v[118:119], s[30:31], v[18:19] op_sel_hi:[1,0,1]
	v_exp_f32_e32 v120, v120
	v_exp_f32_e32 v121, v121
	v_med3_f32 v118, v118, s65, v179
	v_med3_f32 v119, v119, s65, v179
	v_min_f32_e32 v16, 0x40e00000, v16
	v_min_f32_e32 v17, 0x40e00000, v17
	v_rcp_f32_e32 v146, v146
	v_rcp_f32_e32 v147, v147
	v_pk_add_f32 v[120:121], v[120:121], 1.0 op_sel_hi:[1,0]
	v_pk_fma_f32 v[114:115], v[118:119], v[114:115], v[114:115]
	v_pk_mul_f32 v[118:119], v[16:17], s[34:35] op_sel_hi:[1,0]
	v_rcp_f32_e32 v120, v120
	v_rcp_f32_e32 v121, v121
	v_exp_f32_e32 v118, v118
	v_exp_f32_e32 v119, v119
	s_lshr_b32 s39, s39, 1
	v_pk_mul_f32 v[10:11], v[10:11], v[146:147]
	s_lshl_b32 s41, s44, 7
	s_and_b32 s39, s39, 0x60
	v_cvt_pk_fp8_f32 v149, v10, v11 op_sel:[0,0,1]
	v_or_b32_e32 v10, 16, v6
	v_pk_mul_f32 v[114:115], v[114:115], v[120:121]
	v_pk_add_f32 v[118:119], v[118:119], 1.0 op_sel_hi:[1,0]
	v_mov_b32_e32 v120, v167
	s_or_b32 s41, s39, s41
	v_ashrrev_i32_e32 v11, 31, v10
	v_rcp_f32_e32 v118, v118
	v_rcp_f32_e32 v119, v119
	v_cvt_pk_fp8_f32 v120, v14, v15
	v_mov_b32_e32 v121, v167
	v_or_b32_e32 v4, s41, v8
	v_lshlrev_b64 v[10:11], 11, v[10:11]
	v_cvt_pk_fp8_f32 v121, v114, v115
	v_ashrrev_i32_e32 v5, 31, v4
	v_lshl_add_u64 v[10:11], s[16:17], 0, v[10:11]
	v_med3_f32 v116, v116, s65, v179
	v_med3_f32 v117, v117, s65, v179
	v_lshl_add_u64 v[10:11], v[10:11], 0, v[4:5]
	v_pk_fma_f32 v[14:15], v[116:117], v[16:17], v[16:17]
	global_store_dwordx2 v[10:11], v[136:137], off
	v_or_b32_e32 v10, 32, v6
	v_pk_mul_f32 v[14:15], v[14:15], v[118:119]
	v_cvt_pk_fp8_f32 v120, v12, v13 op_sel:[0,0,1]
	v_pk_fma_f32 v[12:13], v[106:107], s[30:31], v[30:31] op_sel_hi:[1,0,1]
	v_ashrrev_i32_e32 v11, 31, v10
	v_cvt_pk_fp8_f32 v121, v14, v15 op_sel:[0,0,1]
	v_min_f32_e32 v12, 0x40e00000, v12
	v_min_f32_e32 v13, 0x40e00000, v13
	v_lshlrev_b64 v[10:11], 11, v[10:11]
	v_pk_mul_f32 v[14:15], v[12:13], s[34:35] op_sel_hi:[1,0]
	v_lshl_add_u64 v[10:11], s[16:17], 0, v[10:11]
	v_exp_f32_e32 v14, v14
	v_exp_f32_e32 v15, v15
	v_lshl_add_u64 v[10:11], v[10:11], 0, v[4:5]
	global_store_dwordx2 v[10:11], v[120:121], off
	v_pk_fma_f32 v[10:11], v[108:109], s[30:31], v[32:33] op_sel_hi:[1,0,1]
	v_pk_add_f32 v[14:15], v[14:15], 1.0 op_sel_hi:[1,0]
	v_min_f32_e32 v10, 0x40e00000, v10
	v_min_f32_e32 v11, 0x40e00000, v11
	v_pk_mul_f32 v[108:109], v[10:11], s[34:35] op_sel_hi:[1,0]
	v_rcp_f32_e32 v14, v14
	v_rcp_f32_e32 v15, v15
	v_exp_f32_e32 v108, v108
	v_exp_f32_e32 v109, v109
	v_pk_fma_f32 v[106:107], v[110:111], s[30:31], v[26:27] op_sel_hi:[1,0,1]
	v_pk_fma_f32 v[16:17], v[112:113], s[30:31], v[28:29] op_sel_hi:[1,0,1]
	v_med3_f32 v106, v106, s65, v179
	v_med3_f32 v107, v107, s65, v179
	v_pk_fma_f32 v[12:13], v[106:107], v[12:13], v[12:13]
	v_med3_f32 v16, v16, s65, v179
	v_pk_mul_f32 v[12:13], v[12:13], v[14:15]
	v_pk_add_f32 v[14:15], v[108:109], 1.0 op_sel_hi:[1,0]
	v_med3_f32 v17, v17, s65, v179
	v_rcp_f32_e32 v14, v14
	v_rcp_f32_e32 v15, v15
	v_pk_fma_f32 v[10:11], v[16:17], v[10:11], v[10:11]
	v_pk_fma_f32 v[16:17], v[90:91], s[30:31], v[22:23] op_sel_hi:[1,0,1]
	v_pk_fma_f32 v[98:99], v[98:99], s[30:31], v[18:19] op_sel_hi:[1,0,1]
	v_min_f32_e32 v16, 0x40e00000, v16
	v_min_f32_e32 v17, 0x40e00000, v17
	v_pk_mul_f32 v[10:11], v[10:11], v[14:15]
	v_pk_fma_f32 v[14:15], v[92:93], s[30:31], v[24:25] op_sel_hi:[1,0,1]
	v_pk_mul_f32 v[92:93], v[16:17], s[34:35] op_sel_hi:[1,0]
	v_med3_f32 v98, v98, s65, v179
	v_exp_f32_e32 v92, v92
	v_exp_f32_e32 v93, v93
	v_med3_f32 v99, v99, s65, v179
	v_min_f32_e32 v14, 0x40e00000, v14
	v_min_f32_e32 v15, 0x40e00000, v15
	v_pk_add_f32 v[92:93], v[92:93], 1.0 op_sel_hi:[1,0]
	v_pk_fma_f32 v[16:17], v[98:99], v[16:17], v[16:17]
	v_pk_mul_f32 v[98:99], v[14:15], s[34:35] op_sel_hi:[1,0]
	v_rcp_f32_e32 v92, v92
	v_rcp_f32_e32 v93, v93
	v_exp_f32_e32 v98, v98
	v_exp_f32_e32 v99, v99
	v_ashrrev_i32_e32 v7, 31, v6
	v_pk_mul_f32 v[16:17], v[16:17], v[92:93]
	v_cvt_pk_fp8_f32 v148, v2, v3 op_sel:[0,0,1]
	v_pk_add_f32 v[92:93], v[98:99], 1.0 op_sel_hi:[1,0]
	v_lshlrev_b64 v[2:3], 11, v[6:7]
	v_or_b32_e32 v6, 48, v6
	v_rcp_f32_e32 v92, v92
	v_rcp_f32_e32 v93, v93
	v_mov_b32_e32 v98, v167
	v_mov_b32_e32 v99, v167
	v_ashrrev_i32_e32 v7, 31, v6
	v_pk_fma_f32 v[90:91], v[100:101], s[30:31], v[20:21] op_sel_hi:[1,0,1]
	v_cvt_pk_fp8_f32 v98, v12, v13
	v_cvt_pk_fp8_f32 v99, v16, v17
	v_med3_f32 v90, v90, s65, v179
	v_med3_f32 v91, v91, s65, v179
	v_lshlrev_b64 v[6:7], 11, v[6:7]
	v_lshl_add_u64 v[2:3], s[16:17], 0, v[2:3]
	v_pk_fma_f32 v[12:13], v[90:91], v[14:15], v[14:15]
	v_lshl_add_u64 v[6:7], s[16:17], 0, v[6:7]
	v_lshl_add_u64 v[2:3], v[2:3], 0, v[4:5]
	v_pk_mul_f32 v[12:13], v[12:13], v[92:93]
	v_lshl_add_u64 v[4:5], v[6:7], 0, v[4:5]
	v_pk_fma_f32 v[6:7], v[94:95], s[30:31], v[30:31] op_sel_hi:[1,0,1]
	v_cvt_pk_fp8_f32 v98, v10, v11 op_sel:[0,0,1]
	v_cvt_pk_fp8_f32 v99, v12, v13 op_sel:[0,0,1]
	v_min_f32_e32 v6, 0x40e00000, v6
	v_min_f32_e32 v7, 0x40e00000, v7
	v_pk_mul_f32 v[10:11], v[6:7], s[34:35] op_sel_hi:[1,0]
	global_store_dwordx2 v[4:5], v[98:99], off
	v_exp_f32_e32 v10, v10
	v_exp_f32_e32 v11, v11
	v_pk_fma_f32 v[4:5], v[96:97], s[30:31], v[32:33] op_sel_hi:[1,0,1]
	v_pk_fma_f32 v[14:15], v[102:103], s[30:31], v[26:27] op_sel_hi:[1,0,1]
	v_min_f32_e32 v4, 0x40e00000, v4
	v_min_f32_e32 v5, 0x40e00000, v5
	v_pk_add_f32 v[10:11], v[10:11], 1.0 op_sel_hi:[1,0]
	v_pk_mul_f32 v[16:17], v[4:5], s[34:35] op_sel_hi:[1,0]
	v_rcp_f32_e32 v10, v10
	v_rcp_f32_e32 v11, v11
	v_exp_f32_e32 v16, v16
	v_exp_f32_e32 v17, v17
	v_pk_fma_f32 v[12:13], v[104:105], s[30:31], v[28:29] op_sel_hi:[1,0,1]
	v_med3_f32 v14, v14, s65, v179
	v_med3_f32 v15, v15, s65, v179
	v_pk_fma_f32 v[6:7], v[14:15], v[6:7], v[6:7]
	v_med3_f32 v12, v12, s65, v179
	v_med3_f32 v13, v13, s65, v179
	v_pk_mul_f32 v[6:7], v[6:7], v[10:11]
	v_pk_add_f32 v[10:11], v[16:17], 1.0 op_sel_hi:[1,0]
	v_pk_fma_f32 v[4:5], v[12:13], v[4:5], v[4:5]
	v_pk_fma_f32 v[12:13], v[82:83], s[30:31], v[22:23] op_sel_hi:[1,0,1]
	v_rcp_f32_e32 v10, v10
	v_rcp_f32_e32 v11, v11
	v_min_f32_e32 v12, 0x40e00000, v12
	v_min_f32_e32 v13, 0x40e00000, v13
	v_pk_mul_f32 v[16:17], v[12:13], s[34:35] op_sel_hi:[1,0]
	v_pk_mul_f32 v[4:5], v[4:5], v[10:11]
	v_exp_f32_e32 v16, v16
	v_exp_f32_e32 v17, v17
	v_pk_fma_f32 v[10:11], v[84:85], s[30:31], v[24:25] op_sel_hi:[1,0,1]
	v_pk_fma_f32 v[82:83], v[86:87], s[30:31], v[18:19] op_sel_hi:[1,0,1]
	v_min_f32_e32 v10, 0x40e00000, v10
	v_med3_f32 v82, v82, s65, v179
	v_med3_f32 v83, v83, s65, v179
	v_min_f32_e32 v11, 0x40e00000, v11
	v_pk_add_f32 v[16:17], v[16:17], 1.0 op_sel_hi:[1,0]
	v_pk_fma_f32 v[12:13], v[82:83], v[12:13], v[12:13]
	v_pk_mul_f32 v[82:83], v[10:11], s[34:35] op_sel_hi:[1,0]
	v_rcp_f32_e32 v16, v16
	v_rcp_f32_e32 v17, v17
	v_exp_f32_e32 v82, v82
	v_exp_f32_e32 v83, v83
	v_pk_fma_f32 v[14:15], v[88:89], s[30:31], v[20:21] op_sel_hi:[1,0,1]
	v_pk_mul_f32 v[12:13], v[12:13], v[16:17]
	v_med3_f32 v14, v14, s65, v179
	v_pk_add_f32 v[16:17], v[82:83], 1.0 op_sel_hi:[1,0]
	v_mov_b32_e32 v83, v167
	v_rcp_f32_e32 v16, v16
	v_rcp_f32_e32 v17, v17
	v_mov_b32_e32 v82, v167
	v_cvt_pk_fp8_f32 v83, v12, v13
	v_med3_f32 v15, v15, s65, v179
	v_cvt_pk_fp8_f32 v82, v6, v7
	v_pk_fma_f32 v[6:7], v[14:15], v[10:11], v[10:11]
	s_mov_b32 s41, 0x40000
	v_pk_mul_f32 v[6:7], v[6:7], v[16:17]
	v_cvt_pk_fp8_f32 v82, v4, v5 op_sel:[0,0,1]
	v_cvt_pk_fp8_f32 v83, v6, v7 op_sel:[0,0,1]
	v_pk_fma_f32 v[6:7], v[74:75], s[30:31], v[30:31] op_sel_hi:[1,0,1]
	v_add_co_u32_e32 v4, vcc, s41, v2
	v_min_f32_e32 v6, 0x40e00000, v6
	v_min_f32_e32 v7, 0x40e00000, v7
	v_pk_mul_f32 v[10:11], v[6:7], s[34:35] op_sel_hi:[1,0]
	v_addc_co_u32_e32 v5, vcc, 0, v3, vcc
	v_exp_f32_e32 v10, v10
	v_exp_f32_e32 v11, v11
	global_store_dwordx2 v[4:5], v[82:83], off
	v_pk_fma_f32 v[4:5], v[76:77], s[30:31], v[32:33] op_sel_hi:[1,0,1]
	v_pk_fma_f32 v[14:15], v[78:79], s[30:31], v[26:27] op_sel_hi:[1,0,1]
	v_min_f32_e32 v4, 0x40e00000, v4
	v_min_f32_e32 v5, 0x40e00000, v5
	v_pk_add_f32 v[10:11], v[10:11], 1.0 op_sel_hi:[1,0]
	v_pk_mul_f32 v[16:17], v[4:5], s[34:35] op_sel_hi:[1,0]
	v_rcp_f32_e32 v10, v10
	v_rcp_f32_e32 v11, v11
	v_exp_f32_e32 v16, v16
	v_exp_f32_e32 v17, v17
	v_pk_fma_f32 v[12:13], v[80:81], s[30:31], v[28:29] op_sel_hi:[1,0,1]
	v_med3_f32 v14, v14, s65, v179
	v_med3_f32 v15, v15, s65, v179
	v_pk_fma_f32 v[6:7], v[14:15], v[6:7], v[6:7]
	v_med3_f32 v12, v12, s65, v179
	v_med3_f32 v13, v13, s65, v179
	v_pk_mul_f32 v[6:7], v[6:7], v[10:11]
	v_pk_add_f32 v[10:11], v[16:17], 1.0 op_sel_hi:[1,0]
	v_pk_fma_f32 v[4:5], v[12:13], v[4:5], v[4:5]
	v_pk_fma_f32 v[12:13], v[66:67], s[30:31], v[22:23] op_sel_hi:[1,0,1]
	v_rcp_f32_e32 v10, v10
	v_rcp_f32_e32 v11, v11
	v_min_f32_e32 v12, 0x40e00000, v12
	v_min_f32_e32 v13, 0x40e00000, v13
	v_pk_mul_f32 v[16:17], v[12:13], s[34:35] op_sel_hi:[1,0]
	v_pk_mul_f32 v[4:5], v[4:5], v[10:11]
	v_exp_f32_e32 v16, v16
	v_exp_f32_e32 v17, v17
	v_pk_fma_f32 v[10:11], v[68:69], s[30:31], v[24:25] op_sel_hi:[1,0,1]
	v_pk_fma_f32 v[66:67], v[70:71], s[30:31], v[18:19] op_sel_hi:[1,0,1]
	v_min_f32_e32 v10, 0x40e00000, v10
	v_med3_f32 v66, v66, s65, v179
	v_med3_f32 v67, v67, s65, v179
	v_min_f32_e32 v11, 0x40e00000, v11
	v_pk_add_f32 v[16:17], v[16:17], 1.0 op_sel_hi:[1,0]
	v_pk_fma_f32 v[12:13], v[66:67], v[12:13], v[12:13]
	v_pk_mul_f32 v[66:67], v[10:11], s[34:35] op_sel_hi:[1,0]
	v_rcp_f32_e32 v16, v16
	v_rcp_f32_e32 v17, v17
	v_exp_f32_e32 v66, v66
	v_exp_f32_e32 v67, v67
	v_pk_fma_f32 v[14:15], v[72:73], s[30:31], v[20:21] op_sel_hi:[1,0,1]
	v_pk_mul_f32 v[12:13], v[12:13], v[16:17]
	v_med3_f32 v14, v14, s65, v179
	v_pk_add_f32 v[16:17], v[66:67], 1.0 op_sel_hi:[1,0]
	v_mov_b32_e32 v67, v167
	v_rcp_f32_e32 v16, v16
	v_rcp_f32_e32 v17, v17
	v_mov_b32_e32 v66, v167
	v_cvt_pk_fp8_f32 v67, v12, v13
	v_med3_f32 v15, v15, s65, v179
	v_cvt_pk_fp8_f32 v66, v6, v7
	v_pk_fma_f32 v[6:7], v[14:15], v[10:11], v[10:11]
	s_mov_b32 s41, 0x48000
	v_pk_mul_f32 v[6:7], v[6:7], v[16:17]
	v_cvt_pk_fp8_f32 v66, v4, v5 op_sel:[0,0,1]
	v_cvt_pk_fp8_f32 v67, v6, v7 op_sel:[0,0,1]
	v_pk_fma_f32 v[6:7], v[58:59], s[30:31], v[30:31] op_sel_hi:[1,0,1]
	v_add_co_u32_e32 v4, vcc, s41, v2
	v_min_f32_e32 v6, 0x40e00000, v6
	v_min_f32_e32 v7, 0x40e00000, v7
	v_pk_mul_f32 v[10:11], v[6:7], s[34:35] op_sel_hi:[1,0]
	v_addc_co_u32_e32 v5, vcc, 0, v3, vcc
	v_exp_f32_e32 v10, v10
	v_exp_f32_e32 v11, v11
	global_store_dwordx2 v[4:5], v[66:67], off
	v_pk_fma_f32 v[4:5], v[60:61], s[30:31], v[32:33] op_sel_hi:[1,0,1]
	v_pk_fma_f32 v[14:15], v[62:63], s[30:31], v[26:27] op_sel_hi:[1,0,1]
	v_min_f32_e32 v4, 0x40e00000, v4
	v_min_f32_e32 v5, 0x40e00000, v5
	v_pk_add_f32 v[10:11], v[10:11], 1.0 op_sel_hi:[1,0]
	v_pk_mul_f32 v[16:17], v[4:5], s[34:35] op_sel_hi:[1,0]
	v_rcp_f32_e32 v10, v10
	v_rcp_f32_e32 v11, v11
	v_exp_f32_e32 v16, v16
	v_exp_f32_e32 v17, v17
	v_pk_fma_f32 v[12:13], v[64:65], s[30:31], v[28:29] op_sel_hi:[1,0,1]
	v_med3_f32 v14, v14, s65, v179
	v_med3_f32 v15, v15, s65, v179
	v_pk_fma_f32 v[6:7], v[14:15], v[6:7], v[6:7]
	v_med3_f32 v12, v12, s65, v179
	v_med3_f32 v13, v13, s65, v179
	v_pk_mul_f32 v[6:7], v[6:7], v[10:11]
	v_pk_add_f32 v[10:11], v[16:17], 1.0 op_sel_hi:[1,0]
	v_pk_fma_f32 v[4:5], v[12:13], v[4:5], v[4:5]
	v_pk_fma_f32 v[12:13], v[50:51], s[30:31], v[22:23] op_sel_hi:[1,0,1]
	v_rcp_f32_e32 v10, v10
	v_rcp_f32_e32 v11, v11
	v_min_f32_e32 v12, 0x40e00000, v12
	v_min_f32_e32 v13, 0x40e00000, v13
	v_pk_mul_f32 v[16:17], v[12:13], s[34:35] op_sel_hi:[1,0]
	v_pk_mul_f32 v[4:5], v[4:5], v[10:11]
	v_exp_f32_e32 v16, v16
	v_exp_f32_e32 v17, v17
	v_pk_fma_f32 v[10:11], v[52:53], s[30:31], v[24:25] op_sel_hi:[1,0,1]
	v_pk_fma_f32 v[50:51], v[54:55], s[30:31], v[18:19] op_sel_hi:[1,0,1]
	v_min_f32_e32 v10, 0x40e00000, v10
	v_med3_f32 v50, v50, s65, v179
	v_med3_f32 v51, v51, s65, v179
	v_min_f32_e32 v11, 0x40e00000, v11
	v_pk_add_f32 v[16:17], v[16:17], 1.0 op_sel_hi:[1,0]
	v_pk_fma_f32 v[12:13], v[50:51], v[12:13], v[12:13]
	v_pk_mul_f32 v[50:51], v[10:11], s[34:35] op_sel_hi:[1,0]
	v_rcp_f32_e32 v16, v16
	v_rcp_f32_e32 v17, v17
	v_exp_f32_e32 v50, v50
	v_exp_f32_e32 v51, v51
	v_pk_fma_f32 v[14:15], v[56:57], s[30:31], v[20:21] op_sel_hi:[1,0,1]
	v_pk_mul_f32 v[12:13], v[12:13], v[16:17]
	v_med3_f32 v14, v14, s65, v179
	v_pk_add_f32 v[16:17], v[50:51], 1.0 op_sel_hi:[1,0]
	v_mov_b32_e32 v51, v167
	v_rcp_f32_e32 v16, v16
	v_rcp_f32_e32 v17, v17
	v_mov_b32_e32 v50, v167
	v_cvt_pk_fp8_f32 v51, v12, v13
	v_med3_f32 v15, v15, s65, v179
	v_cvt_pk_fp8_f32 v50, v6, v7
	v_pk_fma_f32 v[6:7], v[14:15], v[10:11], v[10:11]
	s_mov_b32 s41, 0x50000
	v_pk_mul_f32 v[6:7], v[6:7], v[16:17]
	v_cvt_pk_fp8_f32 v50, v4, v5 op_sel:[0,0,1]
	v_cvt_pk_fp8_f32 v51, v6, v7 op_sel:[0,0,1]
	v_pk_fma_f32 v[6:7], v[42:43], s[30:31], v[30:31] op_sel_hi:[1,0,1]
	v_add_co_u32_e32 v4, vcc, s41, v2
	v_min_f32_e32 v6, 0x40e00000, v6
	v_min_f32_e32 v7, 0x40e00000, v7
	v_pk_mul_f32 v[10:11], v[6:7], s[34:35] op_sel_hi:[1,0]
	v_addc_co_u32_e32 v5, vcc, 0, v3, vcc
	v_exp_f32_e32 v10, v10
	v_exp_f32_e32 v11, v11
	global_store_dwordx2 v[4:5], v[50:51], off
	v_pk_fma_f32 v[4:5], v[44:45], s[30:31], v[32:33] op_sel_hi:[1,0,1]
	v_pk_fma_f32 v[14:15], v[46:47], s[30:31], v[26:27] op_sel_hi:[1,0,1]
	v_min_f32_e32 v4, 0x40e00000, v4
	v_min_f32_e32 v5, 0x40e00000, v5
	v_pk_add_f32 v[10:11], v[10:11], 1.0 op_sel_hi:[1,0]
	v_pk_mul_f32 v[16:17], v[4:5], s[34:35] op_sel_hi:[1,0]
	v_rcp_f32_e32 v10, v10
	v_rcp_f32_e32 v11, v11
	v_exp_f32_e32 v16, v16
	v_exp_f32_e32 v17, v17
	v_pk_fma_f32 v[12:13], v[48:49], s[30:31], v[28:29] op_sel_hi:[1,0,1]
	v_med3_f32 v14, v14, s65, v179
	v_med3_f32 v15, v15, s65, v179
	v_pk_fma_f32 v[6:7], v[14:15], v[6:7], v[6:7]
	v_med3_f32 v12, v12, s65, v179
	v_med3_f32 v13, v13, s65, v179
	v_pk_mul_f32 v[6:7], v[6:7], v[10:11]
	v_pk_add_f32 v[10:11], v[16:17], 1.0 op_sel_hi:[1,0]
	v_pk_fma_f32 v[4:5], v[12:13], v[4:5], v[4:5]
	v_pk_fma_f32 v[12:13], v[34:35], s[30:31], v[22:23] op_sel_hi:[1,0,1]
	v_rcp_f32_e32 v10, v10
	v_rcp_f32_e32 v11, v11
	v_min_f32_e32 v12, 0x40e00000, v12
	v_min_f32_e32 v13, 0x40e00000, v13
	v_pk_mul_f32 v[16:17], v[12:13], s[34:35] op_sel_hi:[1,0]
	v_pk_mul_f32 v[4:5], v[4:5], v[10:11]
	v_exp_f32_e32 v16, v16
	v_exp_f32_e32 v17, v17
	v_pk_fma_f32 v[10:11], v[36:37], s[30:31], v[24:25] op_sel_hi:[1,0,1]
	v_pk_fma_f32 v[18:19], v[38:39], s[30:31], v[18:19] op_sel_hi:[1,0,1]
	v_min_f32_e32 v10, 0x40e00000, v10
	v_med3_f32 v18, v18, s65, v179
	v_med3_f32 v19, v19, s65, v179
	v_min_f32_e32 v11, 0x40e00000, v11
	v_pk_add_f32 v[16:17], v[16:17], 1.0 op_sel_hi:[1,0]
	v_pk_fma_f32 v[12:13], v[18:19], v[12:13], v[12:13]
	v_pk_mul_f32 v[18:19], v[10:11], s[34:35] op_sel_hi:[1,0]
	v_rcp_f32_e32 v16, v16
	v_rcp_f32_e32 v17, v17
	v_exp_f32_e32 v18, v18
	v_exp_f32_e32 v19, v19
	v_pk_fma_f32 v[14:15], v[40:41], s[30:31], v[20:21] op_sel_hi:[1,0,1]
	v_pk_mul_f32 v[12:13], v[12:13], v[16:17]
	v_med3_f32 v14, v14, s65, v179
	v_pk_add_f32 v[16:17], v[18:19], 1.0 op_sel_hi:[1,0]
	v_mov_b32_e32 v18, v167
	v_rcp_f32_e32 v16, v16
	v_rcp_f32_e32 v17, v17
	v_mov_b32_e32 v19, v167
	v_cvt_pk_fp8_f32 v18, v6, v7
	v_cvt_pk_fp8_f32 v19, v12, v13
	v_med3_f32 v15, v15, s65, v179
	v_pk_fma_f32 v[6:7], v[14:15], v[10:11], v[10:11]
	v_cvt_pk_fp8_f32 v18, v4, v5 op_sel:[0,0,1]
	v_pk_mul_f32 v[6:7], v[6:7], v[16:17]
	global_store_dwordx2 v[2:3], v[148:149], off
	v_cvt_pk_fp8_f32 v19, v6, v7 op_sel:[0,0,1]
	v_add_co_u32_e32 v2, vcc, 0x58000, v2
	s_mov_b64 s[44:45], -1
	s_nop 0
	v_addc_co_u32_e32 v3, vcc, 0, v3, vcc
	s_and_b64 vcc, s[42:43], exec
	global_store_dwordx2 v[2:3], v[18:19], off
	s_mov_b32 s100, 1
	s_cbranch_vccz .LBB0_1434
	s_ashr_i32 s41, s40, 31
	s_lshl_b64 s[42:43], s[40:41], 14
	s_add_u32 s41, s88, s42
	s_addc_u32 s44, s89, s43
	s_lshl_b32 s42, s38, 7
	s_ashr_i32 s43, s42, 31
	s_lshl_b64 s[42:43], s[42:43], 2
	s_add_u32 s41, s41, s42
	s_addc_u32 s43, s44, s43
	s_lshl_b32 s39, s39, 2
	s_add_u32 s42, s41, s39
	s_addc_u32 s43, s43, 0
	v_lshlrev_b32_e32 v166, 2, v8
	v_lshl_add_u64 v[2:3], s[42:43], 0, v[166:167]
	v_lshl_add_u64 v[4:5], v[2:3], 0, 16
	s_mov_b64 s[44:45], 0
	global_load_dwordx4 v[30:33], v[2:3], off
	global_load_dwordx4 v[22:25], v[4:5], off
	v_lshl_add_u64 v[4:5], v[2:3], 0, s[12:13]
	global_load_dwordx4 v[26:29], v[4:5], off
	v_lshl_add_u64 v[2:3], v[2:3], 0, s[14:15]
	global_load_dwordx4 v[18:21], v[2:3], off
	s_branch .LBB0_1434

.LBB0_1447:
	v_readfirstlane_b32 s99, v0
	s_cmpk_gt_u32 s99, 0xff
	s_cbranch_scc0 .Lz1x_1442
	s_barrier
